# attention fast loop: first QK MFMA of each step issued right after the step barrier, ahead of the K/V staging block
# baseline (speedup 1.0000x reference)
.LBB0_1629:
	s_or_b64 exec, exec, s[2:3]
	s_mov_b32 s2, 0x40000
	s_nop 1
	v_exp_f32_e32 v174, v4
	v_exp_f32_e32 v176, v5
	s_nop 0
	v_and_b32_e32 v152, 63, v150
	v_lshlrev_b32_e32 v5, 4, v152
	v_exp_f32_e32 v178, v6
	v_lshlrev_b32_e32 v4, 3, v152
	v_and_b32_e32 v5, 0xc0, v5
	v_lshlrev_b32_e32 v6, 1, v152
	v_and_or_b32 v5, v4, 24, v5
	v_and_b32_e32 v6, 32, v6
	v_and_b32_e32 v4, 0x100, v4
	v_or3_b32 v155, v5, v6, v4
	v_bitop3_b32 v4, v151, v150, 15 bitop3:0x78
	s_waitcnt lgkmcnt(0)
	s_barrier
	v_and_b32_e32 v6, 15, v150
	v_lshl_add_u32 v4, v4, 4, v164
	ds_read_b128 v[52:55], v4 offset:16384
	ds_read_b128 v[56:59], v4 offset:24576
	v_bitop3_b32 v4, v151, v6, 2 bitop3:0x36
	v_lshl_add_u32 v4, v4, 4, v164
	ds_read_b128 v[132:135], v4 offset:16384
	ds_read_b128 v[124:127], v4 offset:24576
	v_bitop3_b32 v4, v151, v6, 4 bitop3:0x36
	v_and_b32_e32 v6, 7, v6
	v_lshl_add_u32 v4, v4, 4, v164
	ds_read_b128 v[128:131], v4 offset:16384
	ds_read_b128 v[120:123], v4 offset:24576
	s_lshl_b64 s[20:21], s[36:37], 23
	v_lshlrev_b64 v[4:5], 11, v[28:29]
	v_exp_f32_e32 v180, v7
	v_exp_f32_e32 v182, v8
	v_exp_f32_e32 v184, v9
	v_exp_f32_e32 v186, v10
	v_exp_f32_e32 v187, v11
	v_exp_f32_e32 v175, v12
	v_exp_f32_e32 v177, v13
	v_exp_f32_e32 v179, v14
	v_exp_f32_e32 v181, v15
	v_exp_f32_e32 v183, v16
	v_exp_f32_e32 v185, v17
	v_exp_f32_e32 v188, v18
	v_exp_f32_e32 v189, v19
	v_lshl_add_u64 v[4:5], s[20:21], 0, v[4:5]
	v_lshl_or_b32 v4, v6, 4, v4
	v_lshl_add_u64 v[4:5], v[24:25], 1, v[4:5]
	v_mov_b32_e32 v173, 0
	s_mov_b32 s2, 1
	s_mov_b32 s34, 0
	s_mov_b32 s40, 2
	v_add_u32_e32 v172, 0, v155
	v_mul_hi_u32_u24_e32 v141, 0x2c0, v26
	v_mul_u32_u24_e32 v140, 0x2c0, v26
	v_mul_hi_u32_u24_e32 v143, 0x280, v26
	v_mul_u32_u24_e32 v142, 0x280, v26
	v_mul_hi_u32_u24_e32 v145, 0x240, v26
	v_mul_u32_u24_e32 v144, 0x240, v26
	v_lshlrev_b32_e32 v146, 9, v26
	v_mov_b32_e32 v147, v3
	v_lshl_add_u64 v[148:149], s[14:15], 0, v[4:5]
	s_mov_b32 s3, 0
	s_mov_b32 s41, 1
	s_mov_b32 s43, 2
	s_mov_b32 s42, 1
	v_mov_b32_e32 v4, 0
	v_mov_b32_e32 v5, v173
	v_mov_b32_e32 v6, v173
	v_mov_b32_e32 v7, v173
	v_mov_b32_e32 v8, v173
	v_mov_b32_e32 v9, v173
	v_mov_b32_e32 v10, v173
	v_mov_b32_e32 v11, v173
	v_mov_b32_e32 v12, v173
	v_mov_b32_e32 v13, v173
	v_mov_b32_e32 v14, v173
	v_mov_b32_e32 v15, v173
	v_mov_b32_e32 v16, v173
	v_mov_b32_e32 v17, v173
	v_mov_b32_e32 v18, v173
	v_mov_b32_e32 v19, v173
	v_mov_b32_e32 v20, 0
	v_mov_b32_e32 v21, v173
	v_mov_b32_e32 v22, v173
	v_mov_b32_e32 v23, v173
	v_mov_b32_e32 v24, v173
	v_mov_b32_e32 v25, v173
	v_mov_b32_e32 v26, v173
	v_mov_b32_e32 v27, v173
	v_mov_b32_e32 v28, v173
	v_mov_b32_e32 v29, v173
	v_mov_b32_e32 v30, v173
	v_mov_b32_e32 v31, v173
	v_mov_b32_e32 v32, v173
	v_mov_b32_e32 v33, v173
	v_mov_b32_e32 v34, v173
	v_mov_b32_e32 v35, v173
	s_waitcnt lgkmcnt(0)
.LBB0_1630:
	v_mfma_f32_32x32x16_bf16 v[68:83], v[52:55], v[100:103], 0
	s_mov_b32 s19, s41
	s_mov_b32 s41, s3
	s_mov_b32 s20, s40
	s_mov_b32 s40, s2
	s_and_saveexec_b64 s[2:3], s[38:39]
	s_cbranch_execz .LBB0_1632
	s_lshl_b32 s21, s34, 14
	s_add_i32 s21, s21, 0
	v_add_u32_e32 v60, s21, v154
	v_add_u32_e32 v61, s21, v171
	s_waitcnt vmcnt(1)
	ds_write_b128 v60, v[108:111]
	s_waitcnt vmcnt(0)
	ds_write_b128 v61, v[112:115] offset:8192

.LBB0_1634:
	s_or_b64 exec, exec, s[36:37]
	v_add_co_u32_e32 v60, vcc, 0xfffe0000, v148
	s_nop 1
	v_addc_co_u32_e32 v61, vcc, -1, v149, vcc
	global_load_dwordx4 v[116:119], v[60:61], off
	s_lshl_b32 s21, s40, 14
	s_add_i32 s22, s21, 0
	v_add_u32_e32 v202, s22, v162
	v_add_u32_e32 v60, v202, v168
	ds_read_b128 v[190:193], v60
	s_waitcnt lgkmcnt(7)
	v_add_f32_e32 v52, v174, v176
	v_exp_f32_e32 v204, v36
	v_add_f32_e32 v36, v178, v52
	s_lshl_b32 s21, s41, 13
	v_add_f32_e32 v36, v180, v36
	v_add_u32_e32 v212, s21, v172
	v_exp_f32_e32 v205, v37
	ds_read_b128 v[194:197], v60 offset:8192
	s_waitcnt lgkmcnt(7)
	v_mfma_f32_32x32x16_bf16 v[52:67], v[56:59], v[100:103], 0
	v_add_f32_e32 v36, v182, v36
	v_add_f32_e32 v36, v184, v36
	v_add_f32_e32 v36, v186, v36
	v_add_f32_e32 v36, v187, v36
	v_exp_f32_e32 v206, v38
	v_exp_f32_e32 v207, v39
	v_add_u32_e32 v37, v202, v169
	ds_read_b128 v[198:201], v37
	v_add_f32_e32 v36, v175, v36
	v_add_f32_e32 v36, v177, v36
	v_add_f32_e32 v36, v179, v36
	v_add_f32_e32 v36, v181, v36
	s_waitcnt lgkmcnt(7)
	v_mfma_f32_32x32x16_bf16 v[68:83], v[132:135], v[96:99], v[68:83]
	v_exp_f32_e32 v213, v40
	v_exp_f32_e32 v214, v41
	s_waitcnt lgkmcnt(6)
	v_mfma_f32_32x32x16_bf16 v[52:67], v[124:127], v[96:99], v[52:67]
	ds_read_b128 v[132:135], v37 offset:8192
	v_add_f32_e32 v36, v183, v36
	v_add_f32_e32 v36, v185, v36
	v_add_f32_e32 v36, v188, v36
	v_exp_f32_e32 v215, v42
	v_exp_f32_e32 v218, v43
	v_add_f32_e32 v208, v189, v36
	v_add_u32_e32 v40, v202, v170
	ds_read_b128 v[124:127], v40
	v_exp_f32_e32 v44, v44
	v_exp_f32_e32 v45, v45
	s_waitcnt lgkmcnt(7)
	v_mfma_f32_32x32x16_bf16 v[68:83], v[128:131], v[104:107], v[68:83]
	v_cvt_pk_bf16_f32 v36, v174, v176
	v_cvt_pk_bf16_f32 v37, v178, v180
	v_cvt_pk_bf16_f32 v38, v182, v184
	v_cvt_pk_bf16_f32 v39, v186, v187
	s_waitcnt lgkmcnt(6)
	v_mfma_f32_32x32x16_bf16 v[52:67], v[120:123], v[104:107], v[52:67]
	ds_read_b128 v[128:131], v40 offset:8192
	v_exp_f32_e32 v46, v46
	v_exp_f32_e32 v47, v47
	v_cvt_pk_bf16_f32 v40, v175, v177
	v_cvt_pk_bf16_f32 v41, v179, v181
	v_cvt_pk_bf16_f32 v42, v183, v185
	v_cvt_pk_bf16_f32 v43, v188, v189
	v_exp_f32_e32 v174, v48
	v_exp_f32_e32 v175, v49
	v_permlane32_swap_b32_e32 v36, v38
	v_permlane32_swap_b32_e32 v37, v39
	v_permlane32_swap_b32_e32 v40, v42
	s_waitcnt lgkmcnt(5)
	v_mfma_f32_32x32x16_bf16 v[68:83], v[190:193], v[92:95], v[68:83]
	v_permlane32_swap_b32_e32 v41, v43
	s_waitcnt lgkmcnt(4)
	v_mfma_f32_32x32x16_bf16 v[52:67], v[194:197], v[92:95], v[52:67]
	v_exp_f32_e32 v176, v50
	v_exp_f32_e32 v177, v51
	v_cvt_pk_bf16_f32 v192, v204, v205
	v_cvt_pk_bf16_f32 v193, v206, v207
	v_cvt_pk_bf16_f32 v194, v213, v214
	v_cvt_pk_bf16_f32 v195, v215, v218
	ds_read_b64_tr_b16 v[48:49], v212 offset:49152
	ds_read_b64_tr_b16 v[50:51], v212 offset:50176
	ds_read_b64_tr_b16 v[120:121], v212 offset:49664
	ds_read_b64_tr_b16 v[122:123], v212 offset:50688
	s_waitcnt lgkmcnt(7)
	v_mfma_f32_32x32x16_bf16 v[68:83], v[198:201], v[88:91], v[68:83]
	v_cvt_pk_bf16_f32 v196, v44, v45
	v_cvt_pk_bf16_f32 v197, v46, v47
	v_cvt_pk_bf16_f32 v198, v174, v175
	v_cvt_pk_bf16_f32 v199, v176, v177
	v_permlane32_swap_b32_e32 v192, v194
	v_permlane32_swap_b32_e32 v193, v195
	s_waitcnt lgkmcnt(6)
	v_mfma_f32_32x32x16_bf16 v[52:67], v[132:135], v[88:91], v[52:67]
	ds_read_b64_tr_b16 v[186:187], v212 offset:51200
	ds_read_b64_tr_b16 v[188:189], v212 offset:52224
	ds_read_b64_tr_b16 v[202:203], v212 offset:52736
	ds_read_b64_tr_b16 v[200:201], v212 offset:51712
	v_add_f32_e32 v132, v204, v208
	v_add_f32_e32 v132, v205, v132
	v_add_f32_e32 v132, v206, v132
	v_add_f32_e32 v132, v207, v132
	v_permlane32_swap_b32_e32 v196, v198
	v_permlane32_swap_b32_e32 v197, v199
	ds_read_b64_tr_b16 v[204:205], v212 offset:53248
	ds_read_b64_tr_b16 v[206:207], v212 offset:54272
	ds_read_b64_tr_b16 v[208:209], v212 offset:53760
	ds_read_b64_tr_b16 v[210:211], v212 offset:54784
	s_waitcnt lgkmcnt(13)
	v_mfma_f32_32x32x16_bf16 v[68:83], v[124:127], v[84:87], v[68:83]
	v_add_f32_e32 v124, v213, v132
	v_add_f32_e32 v124, v214, v124
	v_add_f32_e32 v124, v215, v124
	v_add_f32_e32 v124, v218, v124
	v_add_f32_e32 v44, v44, v124
	v_add_f32_e32 v44, v45, v44
	s_waitcnt lgkmcnt(12)
	v_mfma_f32_32x32x16_bf16 v[52:67], v[128:131], v[84:87], v[52:67]
	ds_read_b64_tr_b16 v[218:219], v212 offset:55296
	ds_read_b64_tr_b16 v[220:221], v212 offset:56320
	ds_read_b64_tr_b16 v[224:225], v212 offset:56832
	ds_read_b64_tr_b16 v[222:223], v212 offset:55808
	v_add_f32_e32 v44, v46, v44
	v_add_f32_e32 v44, v47, v44
	v_add_f32_e32 v44, v174, v44
	v_add_f32_e32 v44, v175, v44
	v_add_f32_e32 v44, v176, v44
	v_add_f32_e32 v191, v177, v44
	s_waitcnt lgkmcnt(14)
	v_mfma_f32_32x32x16_bf16 v[4:19], v[36:39], v[48:51], v[4:19]
	v_lshl_add_u32 v174, s20, 14, v164
	v_add_u32_e32 v124, v174, v165
	ds_read_b128 v[44:47], v124
	v_exp_f32_e32 v175, v68
	v_exp_f32_e32 v176, v69
	s_waitcnt lgkmcnt(13)
	v_mfma_f32_32x32x16_bf16 v[20:35], v[36:39], v[120:123], v[20:35]
	ds_read_b128 v[48:51], v124 offset:8192
	v_exp_f32_e32 v178, v70
	v_exp_f32_e32 v180, v71
	s_waitcnt lgkmcnt(12)
	v_mfma_f32_32x32x16_bf16 v[4:19], v[40:43], v[186:189], v[4:19]
	v_add_u32_e32 v36, v174, v166
	ds_read_b128 v[132:135], v36
	v_exp_f32_e32 v183, v72
	v_exp_f32_e32 v184, v73
	s_waitcnt lgkmcnt(11)
	v_mfma_f32_32x32x16_bf16 v[20:35], v[40:43], v[200:203], v[20:35]
	ds_read_b128 v[120:123], v36 offset:8192
	v_exp_f32_e32 v186, v74
	v_exp_f32_e32 v187, v75
	s_waitcnt lgkmcnt(10)
	v_mfma_f32_32x32x16_bf16 v[4:19], v[192:195], v[204:207], v[4:19]
	v_add_u32_e32 v36, v174, v167
	ds_read_b128 v[128:131], v36
	v_exp_f32_e32 v177, v76
	v_exp_f32_e32 v179, v77
	s_waitcnt lgkmcnt(9)
	v_mfma_f32_32x32x16_bf16 v[20:35], v[192:195], v[208:211], v[20:35]
	ds_read_b128 v[124:127], v36 offset:8192
	v_exp_f32_e32 v181, v78
	v_exp_f32_e32 v182, v79
	s_waitcnt lgkmcnt(8)
	v_mfma_f32_32x32x16_bf16 v[4:19], v[196:199], v[218:221], v[4:19]
	v_exp_f32_e32 v185, v80
	v_exp_f32_e32 v188, v81
	s_waitcnt lgkmcnt(6)
	v_mfma_f32_32x32x16_bf16 v[20:35], v[196:199], v[222:225], v[20:35]
	v_exp_f32_e32 v189, v82
	v_exp_f32_e32 v190, v83
	v_mov_b32_e32 v36, v191
	s_nop 1
	v_permlane32_swap_b32_e32 v191, v36
	s_waitcnt lgkmcnt(0)
	s_barrier
	v_mfma_f32_32x32x16_bf16 v[68:83], v[44:47], v[100:103], 0
	s_and_saveexec_b64 s[36:37], s[30:31]
	s_cbranch_execz .LBB0_1636
	v_add_u32_e32 v37, s22, v154
	v_add_u32_e32 v38, s22, v171
	s_waitcnt vmcnt(2)
	ds_write_b128 v37, v[108:111]
	s_waitcnt vmcnt(1)
	ds_write_b128 v38, v[112:115] offset:8192

.LBB0_1640:
	v_add_f32_e32 v36, v191, v36
	v_add_f32_e32 v173, v173, v36
	s_add_i32 s42, s42, 2
	v_add_u32_e32 v36, v174, v168
	ds_read_b128 v[192:195], v36
	v_add_f32_e32 v37, v175, v176
	v_add_f32_e32 v37, v178, v37
	v_add_f32_e32 v37, v180, v37
	v_lshl_add_u32 v212, s19, 13, v172
	s_waitcnt lgkmcnt(7)
	v_exp_f32_e32 v204, v52
	v_exp_f32_e32 v205, v53
	ds_read_b128 v[196:199], v36 offset:8192
	v_add_f32_e32 v36, v183, v37
	v_add_f32_e32 v36, v184, v36
	v_add_f32_e32 v52, v186, v36
	s_waitcnt lgkmcnt(7)
	v_mfma_f32_32x32x16_bf16 v[36:51], v[48:51], v[100:103], 0
	v_exp_f32_e32 v206, v54
	v_exp_f32_e32 v207, v55
	v_add_f32_e32 v191, v187, v52
	v_add_u32_e32 v200, v174, v169
	ds_read_b128 v[52:55], v200
	s_waitcnt lgkmcnt(7)
	v_mfma_f32_32x32x16_bf16 v[68:83], v[132:135], v[96:99], v[68:83]
	v_add_f32_e32 v132, v177, v191
	v_add_f32_e32 v132, v179, v132
	v_add_f32_e32 v132, v181, v132
	v_add_f32_e32 v191, v182, v132
	v_exp_f32_e32 v208, v56
	v_exp_f32_e32 v209, v57
	s_waitcnt lgkmcnt(6)
	v_mfma_f32_32x32x16_bf16 v[36:51], v[120:123], v[96:99], v[36:51]
	ds_read_b128 v[132:135], v200 offset:8192
	v_add_f32_e32 v56, v185, v191
	v_add_f32_e32 v56, v188, v56
	v_add_f32_e32 v56, v189, v56
	v_exp_f32_e32 v210, v58
	v_exp_f32_e32 v211, v59
	v_add_f32_e32 v213, v190, v56
	v_add_u32_e32 v174, v174, v170
	ds_read_b128 v[56:59], v174
	v_cvt_pk_bf16_f32 v120, v175, v176
	v_exp_f32_e32 v175, v60
	v_exp_f32_e32 v176, v61
	s_waitcnt lgkmcnt(7)
	v_mfma_f32_32x32x16_bf16 v[68:83], v[128:131], v[104:107], v[68:83]
	v_cvt_pk_bf16_f32 v121, v178, v180
	v_cvt_pk_bf16_f32 v122, v183, v184
	v_cvt_pk_bf16_f32 v123, v186, v187
	s_waitcnt lgkmcnt(6)
	v_mfma_f32_32x32x16_bf16 v[36:51], v[124:127], v[104:107], v[36:51]
	ds_read_b128 v[200:203], v174 offset:8192
	v_cvt_pk_bf16_f32 v128, v177, v179
	v_exp_f32_e32 v174, v62
	v_exp_f32_e32 v177, v63
	v_cvt_pk_bf16_f32 v129, v181, v182
	v_cvt_pk_bf16_f32 v130, v185, v188
	v_cvt_pk_bf16_f32 v131, v189, v190
	v_exp_f32_e32 v178, v64
	v_exp_f32_e32 v179, v65
	v_permlane32_swap_b32_e32 v120, v122
	v_permlane32_swap_b32_e32 v121, v123
	v_permlane32_swap_b32_e32 v128, v130
	v_permlane32_swap_b32_e32 v129, v131
	s_waitcnt lgkmcnt(5)
	v_mfma_f32_32x32x16_bf16 v[68:83], v[192:195], v[92:95], v[68:83]
	s_waitcnt lgkmcnt(4)
	v_mfma_f32_32x32x16_bf16 v[36:51], v[196:199], v[92:95], v[36:51]
	v_exp_f32_e32 v180, v66
	v_exp_f32_e32 v181, v67
	v_cvt_pk_bf16_f32 v60, v204, v205
	v_cvt_pk_bf16_f32 v61, v206, v207
	v_cvt_pk_bf16_f32 v62, v208, v209
	v_cvt_pk_bf16_f32 v63, v210, v211
	ds_read_b64_tr_b16 v[124:125], v212 offset:49152
	ds_read_b64_tr_b16 v[126:127], v212 offset:50176
	ds_read_b64_tr_b16 v[182:183], v212 offset:49664
	ds_read_b64_tr_b16 v[184:185], v212 offset:50688
	s_waitcnt lgkmcnt(7)
	v_mfma_f32_32x32x16_bf16 v[68:83], v[52:55], v[88:91], v[68:83]
	v_cvt_pk_bf16_f32 v64, v175, v176
	v_cvt_pk_bf16_f32 v65, v174, v177
	v_cvt_pk_bf16_f32 v66, v178, v179
	v_cvt_pk_bf16_f32 v67, v180, v181
	v_permlane32_swap_b32_e32 v60, v62
	v_permlane32_swap_b32_e32 v61, v63
	s_waitcnt lgkmcnt(6)
	v_mfma_f32_32x32x16_bf16 v[36:51], v[132:135], v[88:91], v[36:51]
	ds_read_b64_tr_b16 v[186:187], v212 offset:51200
	ds_read_b64_tr_b16 v[188:189], v212 offset:52224
	ds_read_b64_tr_b16 v[192:193], v212 offset:52736
	ds_read_b64_tr_b16 v[190:191], v212 offset:51712
	v_add_f32_e32 v52, v204, v213
	v_add_f32_e32 v52, v205, v52
	v_add_f32_e32 v52, v206, v52
	v_add_f32_e32 v52, v207, v52
	v_permlane32_swap_b32_e32 v64, v66
	v_permlane32_swap_b32_e32 v65, v67
	ds_read_b64_tr_b16 v[194:195], v212 offset:53248
	ds_read_b64_tr_b16 v[196:197], v212 offset:54272
	ds_read_b64_tr_b16 v[204:205], v212 offset:53760
	ds_read_b64_tr_b16 v[206:207], v212 offset:54784
	v_add_f32_e32 v52, v208, v52
	v_add_f32_e32 v52, v209, v52
	v_add_f32_e32 v52, v210, v52
	v_add_f32_e32 v52, v211, v52
	v_add_f32_e32 v52, v175, v52
	v_add_f32_e32 v52, v176, v52
	s_waitcnt lgkmcnt(13)
	v_mfma_f32_32x32x16_bf16 v[68:83], v[56:59], v[84:87], v[68:83]
	s_waitcnt lgkmcnt(12)
	v_mfma_f32_32x32x16_bf16 v[36:51], v[200:203], v[84:87], v[36:51]
	ds_read_b64_tr_b16 v[208:209], v212 offset:55296
	ds_read_b64_tr_b16 v[210:211], v212 offset:56320
	ds_read_b64_tr_b16 v[220:221], v212 offset:56832
	ds_read_b64_tr_b16 v[218:219], v212 offset:55808
	v_add_f32_e32 v52, v174, v52
	v_add_f32_e32 v52, v177, v52
	v_add_f32_e32 v52, v178, v52
	v_add_f32_e32 v52, v179, v52
	v_add_f32_e32 v52, v180, v52
	v_add_f32_e32 v198, v181, v52
	s_waitcnt lgkmcnt(14)
	v_mfma_f32_32x32x16_bf16 v[4:19], v[120:123], v[124:127], v[4:19]
	v_lshl_add_u32 v179, s34, 14, v164
	v_add_u32_e32 v56, v179, v165
	ds_read_b128 v[52:55], v56
	v_exp_f32_e32 v174, v68
	v_exp_f32_e32 v176, v69
	s_waitcnt lgkmcnt(13)
	v_mfma_f32_32x32x16_bf16 v[20:35], v[120:123], v[182:185], v[20:35]
	ds_read_b128 v[56:59], v56 offset:8192
	v_exp_f32_e32 v178, v70
	v_exp_f32_e32 v180, v71
	s_waitcnt lgkmcnt(12)
	v_mfma_f32_32x32x16_bf16 v[4:19], v[128:131], v[186:189], v[4:19]
	v_add_u32_e32 v68, v179, v166
	ds_read_b128 v[132:135], v68
	v_exp_f32_e32 v182, v72
	v_exp_f32_e32 v184, v73
	s_waitcnt lgkmcnt(11)
	v_mfma_f32_32x32x16_bf16 v[20:35], v[128:131], v[190:193], v[20:35]
	ds_read_b128 v[124:127], v68 offset:8192
	v_exp_f32_e32 v186, v74
	v_exp_f32_e32 v187, v75
	s_waitcnt lgkmcnt(10)
	v_mfma_f32_32x32x16_bf16 v[4:19], v[60:63], v[194:197], v[4:19]
	v_add_u32_e32 v68, v179, v167
	ds_read_b128 v[128:131], v68
	v_exp_f32_e32 v175, v76
	v_exp_f32_e32 v177, v77
	s_waitcnt lgkmcnt(9)
	v_mfma_f32_32x32x16_bf16 v[20:35], v[60:63], v[204:207], v[20:35]
	ds_read_b128 v[120:123], v68 offset:8192
	v_exp_f32_e32 v179, v78
	v_exp_f32_e32 v181, v79
	s_waitcnt lgkmcnt(8)
	v_mfma_f32_32x32x16_bf16 v[4:19], v[64:67], v[208:211], v[4:19]
	v_exp_f32_e32 v183, v80
	v_exp_f32_e32 v185, v81
	s_waitcnt lgkmcnt(6)
	v_mfma_f32_32x32x16_bf16 v[20:35], v[64:67], v[218:221], v[20:35]
	v_exp_f32_e32 v188, v82
	v_exp_f32_e32 v189, v83
	v_mov_b32_e32 v60, v198
	s_nop 1
	v_permlane32_swap_b32_e32 v198, v60
	v_add_f32_e32 v60, v198, v60
	v_add_f32_e32 v173, v173, v60
	s_waitcnt lgkmcnt(0)
	s_barrier
	v_lshl_add_u64 v[138:139], v[138:139], 0, v[2:3]
	v_lshl_add_u64 v[148:149], v[148:149], 0, s[74:75]
	s_and_b64 vcc, exec, s[2:3]
	s_cbranch_vccnz .LBB0_1642
	s_mov_b32 s2, s34
	s_mov_b32 s34, s20
	s_mov_b32 s3, s43
	s_mov_b32 s43, s19
	s_branch .LBB0_1630
